# P0 expert-weight transpose: the 8 waves of a workgroup load the 64x256 f32 block cooperatively, one 1 KB row segment per global_load_dwordx4, cross-wave LDS image with 2 barriers
# speedup vs baseline: 1.0168x; 1.0095x over previous
.LBB0_54:
	s_lshl_b32 s3, s64, 3
	s_add_i32 s3, s3, s76
	s_lshl_b32 s12, s33, 3
	v_and_b32_e32 v2, 63, v38
	s_cmp_gt_i32 s3, 0x1963f
	v_lshlrev_b32_e32 v9, 3, v2
	s_barrier
	s_cbranch_scc1 .LBB0_87
	v_and_b32_e32 v10, 56, v9
	v_mov_b32_e32 v11, 0
	v_lshlrev_b32_e32 v12, 1, v10
	v_mov_b32_e32 v13, v11
	v_lshl_add_u64 v[12:13], s[28:29], 0, v[12:13]
	s_mov_b64 s[6:7], 0x2000000
	v_lshl_add_u64 v[12:13], v[12:13], 0, s[6:7]
	v_lshl_add_u64 v[28:29], s[28:29], 0, v[10:11]
	s_mov_b64 s[6:7], 0xb400000
	s_lshl_b32 s4, s76, 14
	v_lshrrev_b32_e32 v19, 3, v2
	v_lshl_add_u64 v[14:15], v[28:29], 0, s[6:7]
	s_mov_b64 s[6:7], 0x3200000
	s_add_i32 s8, s4, 0
	v_lshrrev_b32_e32 v4, 5, v2
	v_mul_u32_u24_e32 v1, 0x84, v10
	v_lshlrev_b32_e32 v3, 2, v19
	v_lshl_add_u64 v[16:17], v[28:29], 0, s[6:7]
	s_mov_b64 s[6:7], 0x1600000
	v_add3_u32 v23, s8, v1, v3
	v_and_b32_e32 v53, 16, v3
	v_lshl_add_u64 v[20:21], v[28:29], 0, s[6:7]
	s_mov_b64 s[6:7], 0xa00000
	v_mul_u32_u24_e32 v3, 0x84, v4
	v_and_b32_e32 v5, 31, v38
	v_bfe_u32 v52, v2, 3, 2
	v_lshl_add_u64 v[28:29], v[28:29], 0, s[6:7]
	v_or_b32_e32 v3, s4, v3
	s_lshl_b32 s4, s64, 8
	s_lshl_b32 s6, s76, 5
	v_lshlrev_b32_e32 v6, 2, v5
	v_or_b32_e32 v18, v53, v52
	v_mov_b32_e32 v7, v11
	s_add_i32 s14, s4, s6
	s_lshl_b32 s4, s64, 5
	s_lshl_b32 s6, s76, 2
	s_mov_b32 s5, 0
	v_add_u32_e32 v8, s8, v6
	s_movk_i32 s13, 0x84
	v_or_b32_e32 v25, 8, v19
	v_or_b32_e32 v27, 16, v19
	v_or_b32_e32 v39, 24, v19
	v_or_b32_e32 v22, 4, v18
	v_or_b32_e32 v24, 8, v18
	v_or_b32_e32 v26, 12, v18
	v_lshl_add_u64 v[30:31], s[22:23], 0, v[6:7]
	v_mov_b32_e32 v1, v4
	v_add3_u32 v54, v3, v6, 0
	s_lshl_b32 s15, s33, 8
	v_or_b32_e32 v55, 14, v4
	v_or_b32_e32 v56, 12, v4
	v_or_b32_e32 v57, 10, v4
	v_or_b32_e32 v58, 8, v4
	v_or_b32_e32 v59, 6, v4
	v_or_b32_e32 v60, 4, v4
	v_or_b32_e32 v61, 2, v4
	s_add_i32 s16, s4, s6
	s_lshl_b32 s17, s33, 5
	v_lshl_add_u64 v[32:33], s[38:39], 0, v[6:7]
	v_or_b32_e32 v62, 0xfffff80e, v4
	v_or_b32_e32 v63, 0xfffff80c, v4
	v_or_b32_e32 v64, 0xfffff80a, v4
	v_or_b32_e32 v65, 0xfffff808, v4
	v_or_b32_e32 v66, 0xfffff806, v4
	v_or_b32_e32 v67, 0xfffff804, v4
	v_or_b32_e32 v68, 0xfffff802, v4
	v_or_b32_e32 v69, 0xfffff800, v4
	s_movk_i32 s18, 0x7fff
	s_mov_b32 s19, 0xffff0000
	s_mov_b32 s20, 0xc3e00000
	s_movk_i32 s21, 0x3000
	v_mov_b32_e32 v70, 1
	v_mov_b32_e32 v71, 0x43e00000
	v_mov_b32_e32 v72, 0xc2317218
	v_mov_b32_e32 v73, 0xc2b8aa3b
	v_and_b32_e32 v163, 63, v0
	v_lshrrev_b32_e32 v160, 3, v163
	v_and_b32_e32 v161, 7, v163
	v_lshlrev_b32_e32 v161, 4, v161
	v_lshlrev_b32_e32 v163, 4, v163
	v_and_b32_e32 v164, 3, v160
	v_lshrrev_b32_e32 v165, 2, v160
	v_lshl_add_u32 v164, v165, 5, v164
	v_lshlrev_b32_e32 v164, 2, v164
	v_lshl_add_u32 v152, v160, 14, v164
	s_mul_i32 s98, s76, 0x84
	v_add3_u32 v152, v152, v161, s98
	s_and_b32 s98, s76, 3
	s_lshr_b32 s99, s76, 2
	s_lshl_b32 s99, s99, 5
	s_add_i32 s98, s98, s99
	s_lshl_b32 s98, s98, 2
	v_add_u32_e32 v162, s98, v23
	v_add_u32_e32 v153, 0x420, v152
	v_add_u32_e32 v154, 0x840, v152
	v_add_u32_e32 v155, 0xc60, v152
	v_add_u32_e32 v156, 0x1080, v152
	v_add_u32_e32 v157, 0x14a0, v152
	v_add_u32_e32 v158, 0x18c0, v152
	v_add_u32_e32 v159, 0x1ce0, v152
	s_mov_b32 s22, s3
	s_branch .LBB0_57

.LBB0_64:
	s_and_b64 vcc, exec, s[6:7]
	s_cbranch_vccz .LBB0_68
	s_and_b32 s4, s38, 7
	s_lshl_b32 s4, s4, 6
	s_or_b32 s4, s4, s76
	s_lshl_b32 s4, s4, 13
	s_and_b32 s99, s23, 0x1c00
	s_or_b32 s99, s4, s99
	v_add_u32_e32 v144, s99, v163
	s_add_i32 s4, s22, 0xfffeec00
	s_lshl_b32 s6, s4, 13
	s_and_b32 s6, s6, 0xfc00000
	s_add_u32 s6, s40, s6
	s_addc_u32 s7, s41, 0
	s_cmpk_lt_u32 s4, 0x8000
	s_cselect_b32 s7, s7, s37
	s_cselect_b32 s6, s6, s36
	v_add_u32_e32 v145, 0x10000, v144
	v_add_u32_e32 v146, 0x20000, v144
	v_add_u32_e32 v147, 0x30000, v144
	v_add_u32_e32 v148, 0x40000, v144
	v_add_u32_e32 v149, 0x50000, v144
	v_add_u32_e32 v150, 0x60000, v144
	v_add_u32_e32 v151, 0x70000, v144
	global_load_dwordx4 v[112:115], v144, s[6:7] nt
	global_load_dwordx4 v[116:119], v145, s[6:7] nt
	global_load_dwordx4 v[120:123], v146, s[6:7] nt
	global_load_dwordx4 v[124:127], v147, s[6:7] nt
	global_load_dwordx4 v[128:131], v148, s[6:7] nt
	global_load_dwordx4 v[132:135], v149, s[6:7] nt
	global_load_dwordx4 v[136:139], v150, s[6:7] nt
	global_load_dwordx4 v[140:143], v151, s[6:7] nt
	s_barrier
	s_waitcnt vmcnt(7)
	ds_write2_b32 v152, v112, v113 offset1:1
	ds_write2_b32 v152, v114, v115 offset0:2 offset1:3
	s_waitcnt vmcnt(6)
	ds_write2_b32 v153, v116, v117 offset1:1
	ds_write2_b32 v153, v118, v119 offset0:2 offset1:3
	s_waitcnt vmcnt(5)
	ds_write2_b32 v154, v120, v121 offset1:1
	ds_write2_b32 v154, v122, v123 offset0:2 offset1:3
	s_waitcnt vmcnt(4)
	ds_write2_b32 v155, v124, v125 offset1:1
	ds_write2_b32 v155, v126, v127 offset0:2 offset1:3
	s_waitcnt vmcnt(3)
	ds_write2_b32 v156, v128, v129 offset1:1
	ds_write2_b32 v156, v130, v131 offset0:2 offset1:3
	s_waitcnt vmcnt(2)
	ds_write2_b32 v157, v132, v133 offset1:1
	ds_write2_b32 v157, v134, v135 offset0:2 offset1:3
	s_waitcnt vmcnt(1)
	ds_write2_b32 v158, v136, v137 offset1:1
	ds_write2_b32 v158, v138, v139 offset0:2 offset1:3
	s_waitcnt vmcnt(0)
	ds_write2_b32 v159, v140, v141 offset1:1
	ds_write2_b32 v159, v142, v143 offset0:2 offset1:3
	s_waitcnt lgkmcnt(0)
	s_barrier
	s_waitcnt lgkmcnt(0)
	ds_read2_b32 v[34:35], v162 offset1:8
	ds_read2_b32 v[36:37], v162 offset0:33 offset1:41
	ds_read2_b32 v[40:41], v162 offset0:66 offset1:74
	ds_read2_b32 v[42:43], v162 offset0:99 offset1:107
	v_mov_b32_e32 v46, v11
	s_waitcnt lgkmcnt(3)
	v_mul_f32_e32 v3, 0x42800000, v34
	s_waitcnt lgkmcnt(2)
	v_mul_f32_e32 v10, 0x42800000, v36
	v_med3_f32 v3, v3, s20, v71
	v_med3_f32 v10, v10, s20, v71
	v_cvt_pk_fp8_f32 v46, v3, v10
	ds_read2_b32 v[48:49], v162 offset0:132 offset1:140
	ds_read2_b32 v[50:51], v162 offset0:165 offset1:173
	ds_read2_b32 v[74:75], v162 offset0:198 offset1:206
	s_waitcnt lgkmcnt(4)
	v_mul_f32_e32 v34, 0x42800000, v40
	s_waitcnt lgkmcnt(3)
	v_mul_f32_e32 v36, 0x42800000, v42
	v_med3_f32 v34, v34, s20, v71
	v_med3_f32 v3, v36, s20, v71
	ds_read2_b32 v[76:77], v162 offset0:231 offset1:239
	v_cvt_pk_fp8_f32 v46, v34, v3 op_sel:[0,0,1]
	s_waitcnt lgkmcnt(3)
	v_mul_f32_e32 v3, 0x42800000, v48
	s_waitcnt lgkmcnt(2)
	v_mul_f32_e32 v10, 0x42800000, v50
	v_med3_f32 v3, v3, s20, v71
	v_med3_f32 v10, v10, s20, v71
	v_mov_b32_e32 v47, v11
	v_cvt_pk_fp8_f32 v47, v3, v10
	s_waitcnt lgkmcnt(1)
	v_mul_f32_e32 v34, 0x42800000, v74
	s_waitcnt lgkmcnt(0)
	v_mul_f32_e32 v3, 0x42800000, v76
	v_med3_f32 v10, v34, s20, v71
	v_med3_f32 v3, v3, s20, v71
	v_cvt_pk_fp8_f32 v47, v10, v3 op_sel:[0,0,1]
	v_mul_f32_e32 v10, 0x42800000, v35
	v_mul_f32_e32 v34, 0x42800000, v37
	v_med3_f32 v10, v10, s20, v71
	v_med3_f32 v36, v34, s20, v71
	v_mov_b32_e32 v34, v11
	s_lshl_b32 s7, s22, 5
	s_lshr_b32 s4, s4, 9
	v_cvt_pk_fp8_f32 v34, v10, v36
	s_and_b32 s7, s7, 0x700
	s_lshl_b64 s[8:9], s[4:5], 11
	s_and_b32 s6, s22, 0x1c0
	s_or_b32 s4, s8, s7
	s_mov_b32 s7, s5
	v_mul_f32_e32 v35, 0x42800000, v41
	v_mul_f32_e32 v10, 0x42800000, v43
	v_lshl_add_u64 v[44:45], v[14:15], 0, s[6:7]
	s_lshl_b32 s6, s22, 4
	s_lshl_b32 s7, s22, 3
	v_med3_f32 v35, v35, s20, v71
	v_med3_f32 v10, v10, s20, v71
	s_and_b32 s6, s6, 0x60
	s_and_b32 s7, s7, 8
	v_cvt_pk_fp8_f32 v34, v35, v10 op_sel:[0,0,1]
	v_mul_f32_e32 v10, 0x42800000, v49
	v_mul_f32_e32 v35, 0x42800000, v51
	s_or_b32 s6, s7, s6
	v_med3_f32 v10, v10, s20, v71
	v_med3_f32 v37, v35, s20, v71
	v_mov_b32_e32 v35, v11
	v_or_b32_e32 v3, s6, v53
	v_cvt_pk_fp8_f32 v35, v10, v37
	v_or3_b32 v78, v3, v52, s4
	v_mov_b32_e32 v79, s9
	v_lshlrev_b64 v[80:81], 9, v[78:79]
	v_mul_f32_e32 v36, 0x42800000, v75
	v_mul_f32_e32 v10, 0x42800000, v77
	v_lshl_add_u64 v[80:81], v[44:45], 0, v[80:81]
	v_med3_f32 v36, v36, s20, v71
	v_med3_f32 v10, v10, s20, v71
	global_store_dwordx2 v[80:81], v[46:47], off
	v_cvt_pk_fp8_f32 v35, v36, v10 op_sel:[0,0,1]
	v_or_b32_e32 v78, 0x80, v78
	ds_read2_b32 v[40:41], v162 offset0:16 offset1:24
	ds_read2_b32 v[42:43], v162 offset0:49 offset1:57
	ds_read2_b32 v[46:47], v162 offset0:82 offset1:90
	ds_read2_b32 v[48:49], v162 offset0:115 offset1:123
	v_lshlrev_b64 v[36:37], 9, v[78:79]
	v_lshl_add_u64 v[36:37], v[44:45], 0, v[36:37]
	global_store_dwordx2 v[36:37], v[34:35], off
	s_waitcnt lgkmcnt(3)
	v_mul_f32_e32 v10, 0x42800000, v40
	s_waitcnt lgkmcnt(2)
	v_mul_f32_e32 v34, 0x42800000, v42
	v_med3_f32 v10, v10, s20, v71
	v_med3_f32 v36, v34, s20, v71
	v_mov_b32_e32 v34, v11
	v_cvt_pk_fp8_f32 v34, v10, v36
	ds_read2_b32 v[36:37], v162 offset0:148 offset1:156
	ds_read2_b32 v[50:51], v162 offset0:181 offset1:189
	ds_read2_b32 v[74:75], v162 offset0:214 offset1:222
	s_waitcnt lgkmcnt(4)
	v_mul_f32_e32 v35, 0x42800000, v46
	s_waitcnt lgkmcnt(3)
	v_mul_f32_e32 v40, 0x42800000, v48
	v_med3_f32 v35, v35, s20, v71
	v_med3_f32 v10, v40, s20, v71
	ds_read2_b32 v[76:77], v162 offset0:247 offset1:255
	v_cvt_pk_fp8_f32 v34, v35, v10 op_sel:[0,0,1]
	s_waitcnt lgkmcnt(3)
	v_mul_f32_e32 v10, 0x42800000, v36
	s_waitcnt lgkmcnt(2)
	v_mul_f32_e32 v35, 0x42800000, v50
	v_med3_f32 v10, v10, s20, v71
	v_med3_f32 v40, v35, s20, v71
	v_mov_b32_e32 v35, v11
	v_cvt_pk_fp8_f32 v35, v10, v40
	s_waitcnt lgkmcnt(1)
	v_mul_f32_e32 v36, 0x42800000, v74
	s_waitcnt lgkmcnt(0)
	v_mul_f32_e32 v10, 0x42800000, v76
	v_med3_f32 v36, v36, s20, v71
	v_med3_f32 v10, v10, s20, v71
	v_cvt_pk_fp8_f32 v35, v36, v10 op_sel:[0,0,1]
	v_or3_b32 v3, v3, v19, s4
	v_or_b32_e32 v78, 4, v3
	v_lshlrev_b64 v[80:81], 9, v[78:79]
	v_lshl_add_u64 v[80:81], v[44:45], 0, v[80:81]
	global_store_dwordx2 v[80:81], v[34:35], off
	v_mul_f32_e32 v34, 0x42800000, v41
	v_med3_f32 v35, v34, s20, v71
	v_mul_f32_e32 v34, 0x42800000, v43
	v_med3_f32 v36, v34, s20, v71
	v_mov_b32_e32 v34, v11
	v_cvt_pk_fp8_f32 v34, v35, v36
	v_mul_f32_e32 v10, 0x42800000, v47
	v_mul_f32_e32 v35, 0x42800000, v49
	v_med3_f32 v10, v10, s20, v71
	v_med3_f32 v35, v35, s20, v71
	v_cvt_pk_fp8_f32 v34, v10, v35 op_sel:[0,0,1]
	v_mul_f32_e32 v35, 0x42800000, v37
	v_med3_f32 v36, v35, s20, v71
	v_mul_f32_e32 v35, 0x42800000, v51
	v_med3_f32 v37, v35, s20, v71
	v_mov_b32_e32 v35, v11
	v_cvt_pk_fp8_f32 v35, v36, v37
	v_mul_f32_e32 v10, 0x42800000, v75
	v_mul_f32_e32 v36, 0x42800000, v77
	v_med3_f32 v10, v10, s20, v71
	v_med3_f32 v36, v36, s20, v71
	v_cvt_pk_fp8_f32 v35, v10, v36 op_sel:[0,0,1]
	v_or_b32_e32 v78, 0x84, v3
	v_lshlrev_b64 v[36:37], 9, v[78:79]
	v_lshl_add_u64 v[36:37], v[44:45], 0, v[36:37]
	global_store_dwordx2 v[36:37], v[34:35], off
	s_waitcnt lgkmcnt(0)

.LBB0_74:
	s_lshr_b32 s4, s14, 5
	s_and_b32 s4, s4, 8
	s_and_b32 s8, s16, 0x7c0
	s_lshl_b32 s4, s4, 7
	s_or_b32 s8, s8, s76
	s_lshl_b32 s8, s8, 11
	s_or_b32 s8, s8, s4
	v_add_u32_e32 v144, s8, v163
	s_waitcnt lgkmcnt(0)
	v_add_u32_e32 v145, 0x4000, v144
	v_add_u32_e32 v146, 0x8000, v144
	v_add_u32_e32 v147, 0xc000, v144
	v_add_u32_e32 v148, 0x10000, v144
	v_add_u32_e32 v149, 0x14000, v144
	v_add_u32_e32 v150, 0x18000, v144
	v_add_u32_e32 v151, 0x1c000, v144
	global_load_dwordx4 v[112:115], v144, s[6:7] nt
	global_load_dwordx4 v[116:119], v145, s[6:7] nt
	global_load_dwordx4 v[120:123], v146, s[6:7] nt
	global_load_dwordx4 v[124:127], v147, s[6:7] nt
	global_load_dwordx4 v[128:131], v148, s[6:7] nt
	global_load_dwordx4 v[132:135], v149, s[6:7] nt
	global_load_dwordx4 v[136:139], v150, s[6:7] nt
	global_load_dwordx4 v[140:143], v151, s[6:7] nt
	s_barrier
	s_waitcnt vmcnt(7)
	ds_write2_b32 v152, v112, v113 offset1:1
	ds_write2_b32 v152, v114, v115 offset0:2 offset1:3
	s_waitcnt vmcnt(6)
	ds_write2_b32 v153, v116, v117 offset1:1
	ds_write2_b32 v153, v118, v119 offset0:2 offset1:3
	s_waitcnt vmcnt(5)
	ds_write2_b32 v154, v120, v121 offset1:1
	ds_write2_b32 v154, v122, v123 offset0:2 offset1:3
	s_waitcnt vmcnt(4)
	ds_write2_b32 v155, v124, v125 offset1:1
	ds_write2_b32 v155, v126, v127 offset0:2 offset1:3
	s_waitcnt vmcnt(3)
	ds_write2_b32 v156, v128, v129 offset1:1
	ds_write2_b32 v156, v130, v131 offset0:2 offset1:3
	s_waitcnt vmcnt(2)
	ds_write2_b32 v157, v132, v133 offset1:1
	ds_write2_b32 v157, v134, v135 offset0:2 offset1:3
	s_waitcnt vmcnt(1)
	ds_write2_b32 v158, v136, v137 offset1:1
	ds_write2_b32 v158, v138, v139 offset0:2 offset1:3
	s_waitcnt vmcnt(0)
	ds_write2_b32 v159, v140, v141 offset1:1
	ds_write2_b32 v159, v142, v143 offset0:2 offset1:3
	s_waitcnt lgkmcnt(0)
	s_barrier
	s_lshl_b32 s6, s22, 5
	s_lshl_b32 s4, s22, 2
	s_lshl_b32 s7, s22, 6
	s_waitcnt lgkmcnt(0)
	s_and_b32 s4, s4, 0x7c0
	s_and_b32 s7, s7, 0x300
	s_and_b32 s6, s6, 0x60
	s_lshl_b32 s8, s42, 7
	s_cmp_eq_u32 s42, 0
	ds_read2_b32 v[34:35], v162 offset1:8
	ds_read2_b32 v[36:37], v162 offset0:33 offset1:41
	ds_read2_b32 v[40:41], v162 offset0:66 offset1:74
	ds_read2_b32 v[42:43], v162 offset0:99 offset1:107
	s_cselect_b64 vcc, -1, 0
	v_cndmask_b32_e32 v3, v72, v73, vcc
	s_waitcnt lgkmcnt(3)
	v_mul_f32_e32 v10, v3, v34
	s_waitcnt lgkmcnt(2)
	v_mul_f32_e32 v34, v3, v36
	v_med3_f32 v10, v10, s20, v71
	v_med3_f32 v34, v34, s20, v71
	v_mov_b32_e32 v46, v11
	v_cvt_pk_fp8_f32 v46, v10, v34
	ds_read2_b32 v[48:49], v162 offset0:132 offset1:140
	ds_read2_b32 v[50:51], v162 offset0:165 offset1:173
	ds_read2_b32 v[74:75], v162 offset0:198 offset1:206
	s_waitcnt lgkmcnt(4)
	v_mul_f32_e32 v36, v3, v40
	s_waitcnt lgkmcnt(3)
	v_mul_f32_e32 v40, v3, v42
	v_med3_f32 v36, v36, s20, v71
	v_med3_f32 v10, v40, s20, v71
	ds_read2_b32 v[76:77], v162 offset0:231 offset1:239
	v_cvt_pk_fp8_f32 v46, v36, v10 op_sel:[0,0,1]
	s_waitcnt lgkmcnt(3)
	v_mul_f32_e32 v10, v3, v48
	s_waitcnt lgkmcnt(2)
	v_mul_f32_e32 v34, v3, v50
	v_med3_f32 v10, v10, s20, v71
	v_med3_f32 v34, v34, s20, v71
	v_mov_b32_e32 v47, v11
	v_cvt_pk_fp8_f32 v47, v10, v34
	s_waitcnt lgkmcnt(1)
	v_mul_f32_e32 v36, v3, v74
	s_waitcnt lgkmcnt(0)
	v_mul_f32_e32 v10, v3, v76
	v_med3_f32 v34, v36, s20, v71
	v_med3_f32 v10, v10, s20, v71
	v_cvt_pk_fp8_f32 v47, v34, v10 op_sel:[0,0,1]
	v_mul_f32_e32 v34, v3, v35
	v_mul_f32_e32 v35, v3, v37
	v_med3_f32 v37, v34, s20, v71
	v_med3_f32 v35, v35, s20, v71
	v_mov_b32_e32 v34, v11
	v_cvt_pk_fp8_f32 v34, v37, v35
	v_mul_f32_e32 v36, v3, v41
	v_mul_f32_e32 v35, v3, v43
	s_and_b32 s9, s39, 0xfffffc00
	v_med3_f32 v36, v36, s20, v71
	v_med3_f32 v35, v35, s20, v71
	s_or_b32 s7, s9, s7
	v_cvt_pk_fp8_f32 v34, v36, v35 op_sel:[0,0,1]
	v_mul_f32_e32 v35, v3, v49
	v_mul_f32_e32 v36, v3, v51
	s_or_b32 s7, s7, s8
	v_med3_f32 v40, v35, s20, v71
	v_med3_f32 v36, v36, s20, v71
	v_mov_b32_e32 v35, v11
	s_or_b32 s6, s7, s6
	v_cvt_pk_fp8_f32 v35, v40, v36
	v_or_b32_e32 v10, s6, v18
	v_lshl_add_u64 v[44:45], v[16:17], 0, s[4:5]
	v_lshlrev_b64 v[78:79], 11, v[10:11]
	v_mul_f32_e32 v37, v3, v75
	v_mul_f32_e32 v36, v3, v77
	v_lshl_add_u64 v[78:79], v[44:45], 0, v[78:79]
	v_med3_f32 v37, v37, s20, v71
	v_med3_f32 v36, v36, s20, v71
	global_store_dwordx2 v[78:79], v[46:47], off
	v_cvt_pk_fp8_f32 v35, v37, v36 op_sel:[0,0,1]
	v_or_b32_e32 v36, 4, v10
	v_mov_b32_e32 v37, v11
	ds_read2_b32 v[40:41], v162 offset0:16 offset1:24
	ds_read2_b32 v[42:43], v162 offset0:49 offset1:57
	ds_read2_b32 v[46:47], v162 offset0:82 offset1:90
	ds_read2_b32 v[48:49], v162 offset0:115 offset1:123
	v_lshlrev_b64 v[36:37], 11, v[36:37]
	v_lshl_add_u64 v[36:37], v[44:45], 0, v[36:37]
	global_store_dwordx2 v[36:37], v[34:35], off
	s_waitcnt lgkmcnt(3)
	v_mul_f32_e32 v34, v3, v40
	s_waitcnt lgkmcnt(2)
	v_mul_f32_e32 v35, v3, v42
	s_waitcnt lgkmcnt(1)
	v_mul_f32_e32 v36, v3, v46
	v_med3_f32 v37, v34, s20, v71
	v_med3_f32 v35, v35, s20, v71
	v_mov_b32_e32 v34, v11
	v_med3_f32 v42, v36, s20, v71
	v_cvt_pk_fp8_f32 v34, v37, v35
	ds_read2_b32 v[36:37], v162 offset0:148 offset1:156
	ds_read2_b32 v[50:51], v162 offset0:181 offset1:189
	ds_read2_b32 v[74:75], v162 offset0:214 offset1:222
	s_waitcnt lgkmcnt(3)
	v_mul_f32_e32 v40, v3, v48
	v_med3_f32 v35, v40, s20, v71
	ds_read2_b32 v[76:77], v162 offset0:247 offset1:255
	v_cvt_pk_fp8_f32 v34, v42, v35 op_sel:[0,0,1]
	s_waitcnt lgkmcnt(3)
	v_mul_f32_e32 v35, v3, v36
	s_waitcnt lgkmcnt(2)
	v_mul_f32_e32 v36, v3, v50
	v_med3_f32 v42, v35, s20, v71
	v_med3_f32 v36, v36, s20, v71
	v_mov_b32_e32 v35, v11
	v_cvt_pk_fp8_f32 v35, v42, v36
	s_waitcnt lgkmcnt(1)
	v_mul_f32_e32 v40, v3, v74
	s_waitcnt lgkmcnt(0)
	v_mul_f32_e32 v36, v3, v76
	v_med3_f32 v40, v40, s20, v71
	v_med3_f32 v36, v36, s20, v71
	v_cvt_pk_fp8_f32 v35, v40, v36 op_sel:[0,0,1]
	v_or_b32_e32 v78, 8, v10
	v_mov_b32_e32 v79, v11
	v_lshlrev_b64 v[78:79], 11, v[78:79]
	v_lshl_add_u64 v[78:79], v[44:45], 0, v[78:79]
	global_store_dwordx2 v[78:79], v[34:35], off
	v_mul_f32_e32 v34, v3, v41
	v_med3_f32 v36, v34, s20, v71
	v_mul_f32_e32 v34, v3, v43
	v_med3_f32 v40, v34, s20, v71
	v_mov_b32_e32 v34, v11
	v_cvt_pk_fp8_f32 v34, v36, v40
	v_mul_f32_e32 v35, v3, v47
	v_mul_f32_e32 v36, v3, v49
	v_med3_f32 v35, v35, s20, v71
	v_med3_f32 v36, v36, s20, v71
	v_cvt_pk_fp8_f32 v34, v35, v36 op_sel:[0,0,1]
	v_mul_f32_e32 v35, v3, v37
	v_med3_f32 v37, v35, s20, v71
	v_mul_f32_e32 v35, v3, v51
	v_med3_f32 v40, v35, s20, v71
	v_mov_b32_e32 v35, v11
	v_cvt_pk_fp8_f32 v35, v37, v40
	v_mul_f32_e32 v36, v3, v75
	v_mul_f32_e32 v3, v3, v77
	v_med3_f32 v36, v36, s20, v71
	v_med3_f32 v3, v3, s20, v71
	v_cvt_pk_fp8_f32 v35, v36, v3 op_sel:[0,0,1]
	v_or_b32_e32 v10, 12, v10
	v_lshlrev_b64 v[36:37], 11, v[10:11]
	v_lshl_add_u64 v[36:37], v[44:45], 0, v[36:37]
	global_store_dwordx2 v[36:37], v[34:35], off
	s_waitcnt lgkmcnt(0)
